# MoE queue prefix tables rewritten by hand: expert tile counts preloaded once, straight-line prefix sums (no LDS round trip per slot)
# speedup vs baseline: 1.0215x; 1.0100x over previous
; #define LAS3 __attribute__((address_space(3)))
; __device__ __forceinline__ int lane_id() { int r; asm volatile("v_mbcnt_lo_u32_b32 %0, -1, 0\n\tv_mbcnt_hi_u32_b32 %0, -1, %0" : "=v"(r)); return r; }
; template <int EPI>
; __device__ __forceinline__ int* moe_phase(const Params& p, LAS3 char* lds, int wid, int* pend_in) {
;     ...
;     { const int t0 = wid * 64 + lane_id();
;       if (t0 < 8) { int a = 0; LAS3 int* pq = pre + t0 * 128;
;           for (int s = 0; s <= NSL; ++s) { pq[s] = a;
;               if (s < NSL) { int nv = (s < NS && mtv[t0 + 8 * (s / NCOL)] > 0) ? 1 : 0; const int sc = s - MOE_LAG;
;                   if (EPI == 2 && s < MOE_LAG3 && mtv[t0 + 8 * (s >> 3)] > 0) nv += 1;
;                   if (sc >= 0 && sc < NS) nv += mtv[t0 + 8 * (sc / NCOL)];
;                   a += nv; } } } }
.LBB0_410:
	s_or_b64 exec, exec, s[0:1]
	v_mbcnt_lo_u32_b32 v2, -1, 0
	v_mbcnt_hi_u32_b32 v2, -1, v2
	s_nop 0
	v_add_u32_e32 v0, s75, v2
	v_cmp_gt_i32_e32 vcc, 8, v0
	s_and_saveexec_b64 s[0:1], vcc
	s_cbranch_execz .LBB0_428
	s_waitcnt vmcnt(0)
	v_lshl_add_u32 v1, v0, 9, 0
	v_add_u32_e32 v1, 0x22000, v1
	v_lshl_add_u32 v3, v0, 2, 0
	v_add_u32_e32 v3, 0x21300, v3
	ds_read_b32 v4, v3
	ds_read_b32 v5, v3 offset:32
	ds_read_b32 v6, v3 offset:64
	ds_read_b32 v7, v3 offset:96
	v_mov_b32_e32 v2, 0
	s_waitcnt lgkmcnt(0)
	v_cmp_lt_i32_e32 vcc, 0, v4
	s_nop 1
	v_cndmask_b32_e64 v3, 0, 1, vcc
	ds_write_b32 v1, v2
	v_add_u32_e32 v2, v2, v3
	ds_write_b32 v1, v2 offset:4
	v_add_u32_e32 v2, v2, v3
	ds_write_b32 v1, v2 offset:8
	v_add_u32_e32 v2, v2, v3
	ds_write_b32 v1, v2 offset:12
	v_add_u32_e32 v2, v2, v3
	ds_write_b32 v1, v2 offset:16
	v_add_u32_e32 v2, v2, v3
	ds_write_b32 v1, v2 offset:20
	v_add_u32_e32 v2, v2, v3
	ds_write_b32 v1, v2 offset:24
	v_add_u32_e32 v2, v2, v3
	ds_write_b32 v1, v2 offset:28
	v_add_u32_e32 v2, v2, v3
	ds_write_b32 v1, v2 offset:32
	v_add_u32_e32 v2, v2, v3
	ds_write_b32 v1, v2 offset:36
	v_add_u32_e32 v2, v2, v3
	ds_write_b32 v1, v2 offset:40
	v_add_u32_e32 v2, v2, v3
	ds_write_b32 v1, v2 offset:44
	v_add_u32_e32 v2, v2, v3
	ds_write_b32 v1, v2 offset:48
	v_add_u32_e32 v2, v2, v3
	ds_write_b32 v1, v2 offset:52
	v_add_u32_e32 v2, v2, v3
	ds_write_b32 v1, v2 offset:56
	v_add_u32_e32 v2, v2, v3
	v_cmp_lt_i32_e32 vcc, 0, v4
	s_nop 1
	v_addc_co_u32_e32 v3, vcc, 0, v4, vcc
	ds_write_b32 v1, v2 offset:60
	v_add_u32_e32 v2, v2, v3
	v_cmp_lt_i32_e32 vcc, 0, v5
	s_nop 1
	v_addc_co_u32_e32 v3, vcc, 0, v4, vcc
	ds_write_b32 v1, v2 offset:64
	v_add_u32_e32 v2, v2, v3
	ds_write_b32 v1, v2 offset:68
	v_add_u32_e32 v2, v2, v3
	ds_write_b32 v1, v2 offset:72
	v_add_u32_e32 v2, v2, v3
	ds_write_b32 v1, v2 offset:76
	v_add_u32_e32 v2, v2, v3
	ds_write_b32 v1, v2 offset:80
	v_add_u32_e32 v2, v2, v3
	ds_write_b32 v1, v2 offset:84
	v_add_u32_e32 v2, v2, v3
	ds_write_b32 v1, v2 offset:88
	v_add_u32_e32 v2, v2, v3
	ds_write_b32 v1, v2 offset:92
	v_add_u32_e32 v2, v2, v3
	ds_write_b32 v1, v2 offset:96
	v_add_u32_e32 v2, v2, v3
	ds_write_b32 v1, v2 offset:100
	v_add_u32_e32 v2, v2, v3
	ds_write_b32 v1, v2 offset:104
	v_add_u32_e32 v2, v2, v3
	ds_write_b32 v1, v2 offset:108
	v_add_u32_e32 v2, v2, v3
	ds_write_b32 v1, v2 offset:112
	v_add_u32_e32 v2, v2, v3
	ds_write_b32 v1, v2 offset:116
	v_add_u32_e32 v2, v2, v3
	ds_write_b32 v1, v2 offset:120
	v_add_u32_e32 v2, v2, v3
	v_cmp_lt_i32_e32 vcc, 0, v5
	s_nop 1
	v_addc_co_u32_e32 v3, vcc, 0, v5, vcc
	ds_write_b32 v1, v2 offset:124
	v_add_u32_e32 v2, v2, v3
	v_cmp_lt_i32_e32 vcc, 0, v6
	s_nop 1
	v_addc_co_u32_e32 v3, vcc, 0, v5, vcc
	ds_write_b32 v1, v2 offset:128
	v_add_u32_e32 v2, v2, v3
	ds_write_b32 v1, v2 offset:132
	v_add_u32_e32 v2, v2, v3
	ds_write_b32 v1, v2 offset:136
	v_add_u32_e32 v2, v2, v3
	ds_write_b32 v1, v2 offset:140
	v_add_u32_e32 v2, v2, v3
	ds_write_b32 v1, v2 offset:144
	v_add_u32_e32 v2, v2, v3
	ds_write_b32 v1, v2 offset:148
	v_add_u32_e32 v2, v2, v3
	ds_write_b32 v1, v2 offset:152
	v_add_u32_e32 v2, v2, v3
	ds_write_b32 v1, v2 offset:156
	v_add_u32_e32 v2, v2, v3
	ds_write_b32 v1, v2 offset:160
	v_add_u32_e32 v2, v2, v3
	ds_write_b32 v1, v2 offset:164
	v_add_u32_e32 v2, v2, v3
	ds_write_b32 v1, v2 offset:168
	v_add_u32_e32 v2, v2, v3
	ds_write_b32 v1, v2 offset:172
	v_add_u32_e32 v2, v2, v3
	ds_write_b32 v1, v2 offset:176
	v_add_u32_e32 v2, v2, v3
	ds_write_b32 v1, v2 offset:180
	v_add_u32_e32 v2, v2, v3
	ds_write_b32 v1, v2 offset:184
	v_add_u32_e32 v2, v2, v3
	v_cmp_lt_i32_e32 vcc, 0, v6
	s_nop 1
	v_addc_co_u32_e32 v3, vcc, 0, v6, vcc
	ds_write_b32 v1, v2 offset:188
	v_add_u32_e32 v2, v2, v3
	v_cmp_lt_i32_e32 vcc, 0, v7
	s_nop 1
	v_addc_co_u32_e32 v3, vcc, 0, v6, vcc
	ds_write_b32 v1, v2 offset:192
	v_add_u32_e32 v2, v2, v3
	ds_write_b32 v1, v2 offset:196
	v_add_u32_e32 v2, v2, v3
	ds_write_b32 v1, v2 offset:200
	v_add_u32_e32 v2, v2, v3
	ds_write_b32 v1, v2 offset:204
	v_add_u32_e32 v2, v2, v3
	ds_write_b32 v1, v2 offset:208
	v_add_u32_e32 v2, v2, v3
	ds_write_b32 v1, v2 offset:212
	v_add_u32_e32 v2, v2, v3
	ds_write_b32 v1, v2 offset:216
	v_add_u32_e32 v2, v2, v3
	ds_write_b32 v1, v2 offset:220
	v_add_u32_e32 v2, v2, v3
	ds_write_b32 v1, v2 offset:224
	v_add_u32_e32 v2, v2, v3
	ds_write_b32 v1, v2 offset:228
	v_add_u32_e32 v2, v2, v3
	ds_write_b32 v1, v2 offset:232
	v_add_u32_e32 v2, v2, v3
	ds_write_b32 v1, v2 offset:236
	v_add_u32_e32 v2, v2, v3
	ds_write_b32 v1, v2 offset:240
	v_add_u32_e32 v2, v2, v3
	ds_write_b32 v1, v2 offset:244
	v_add_u32_e32 v2, v2, v3
	ds_write_b32 v1, v2 offset:248
	v_add_u32_e32 v2, v2, v3
	v_cmp_lt_i32_e32 vcc, 0, v7
	s_nop 1
	v_addc_co_u32_e32 v3, vcc, 0, v7, vcc
	ds_write_b32 v1, v2 offset:252
	v_add_u32_e32 v2, v2, v3
	v_mov_b32_e32 v3, v7
	ds_write_b32 v1, v2 offset:256
	v_add_u32_e32 v2, v2, v3
	ds_write_b32 v1, v2 offset:260
	v_add_u32_e32 v2, v2, v3
	ds_write_b32 v1, v2 offset:264
	v_add_u32_e32 v2, v2, v3
	ds_write_b32 v1, v2 offset:268
	v_add_u32_e32 v2, v2, v3
	ds_write_b32 v1, v2 offset:272
	v_add_u32_e32 v2, v2, v3
	ds_write_b32 v1, v2 offset:276
	v_add_u32_e32 v2, v2, v3
	ds_write_b32 v1, v2 offset:280
	v_add_u32_e32 v2, v2, v3
	ds_write_b32 v1, v2 offset:284
	v_add_u32_e32 v2, v2, v3
	ds_write_b32 v1, v2 offset:288
	v_add_u32_e32 v2, v2, v3
	ds_write_b32 v1, v2 offset:292
	v_add_u32_e32 v2, v2, v3
	ds_write_b32 v1, v2 offset:296
	v_add_u32_e32 v2, v2, v3
	ds_write_b32 v1, v2 offset:300
	v_add_u32_e32 v2, v2, v3
	ds_write_b32 v1, v2 offset:304
	v_add_u32_e32 v2, v2, v3
	ds_write_b32 v1, v2 offset:308
	v_add_u32_e32 v2, v2, v3
	ds_write_b32 v1, v2 offset:312
	v_add_u32_e32 v2, v2, v3
	ds_write_b32 v1, v2 offset:316

; #define LAS3 __attribute__((address_space(3)))
; __device__ __forceinline__ int lane_id() { int r; asm volatile("v_mbcnt_lo_u32_b32 %0, -1, 0\n\tv_mbcnt_hi_u32_b32 %0, -1, %0" : "=v"(r)); return r; }
; template <int EPI>
; __device__ __forceinline__ int* moe_phase(const Params& p, LAS3 char* lds, int wid, int* pend_in) {
;     ...
;     { const int t0 = wid * 64 + lane_id();
;       if (t0 < 8) { int a = 0; LAS3 int* pq = pre + t0 * 128;
;           for (int s = 0; s <= NSL; ++s) { pq[s] = a;
;               if (s < NSL) { int nv = (s < NS && mtv[t0 + 8 * (s / NCOL)] > 0) ? 1 : 0; const int sc = s - MOE_LAG;
;                   if (EPI == 2 && s < MOE_LAG3 && mtv[t0 + 8 * (s >> 3)] > 0) nv += 1;
;                   if (sc >= 0 && sc < NS) nv += mtv[t0 + 8 * (sc / NCOL)];
;                   a += nv; } } } }
.LBB0_514:
	s_or_b64 exec, exec, s[0:1]
	v_mbcnt_lo_u32_b32 v0, -1, 0
	v_mbcnt_hi_u32_b32 v0, -1, v0
	s_nop 0
	v_add_u32_e32 v0, s75, v0
	v_cmp_gt_i32_e32 vcc, 8, v0
	s_and_saveexec_b64 s[0:1], vcc
	s_cbranch_execz .LBB0_516
	s_waitcnt vmcnt(0)
	v_lshl_add_u32 v1, v0, 9, 0
	v_add_u32_e32 v1, 0x22000, v1
	v_lshl_add_u32 v3, v0, 2, 0
	v_add_u32_e32 v3, 0x21300, v3
	ds_read_b32 v4, v3
	ds_read_b32 v5, v3 offset:32
	ds_read_b32 v6, v3 offset:64
	ds_read_b32 v7, v3 offset:96
	v_mov_b32_e32 v2, 0
	s_waitcnt lgkmcnt(0)
	v_cmp_lt_i32_e32 vcc, 0, v4
	s_nop 1
	v_cndmask_b32_e64 v3, 0, 1, vcc
	ds_write_b32 v1, v2
	v_add_u32_e32 v2, v2, v3
	ds_write_b32 v1, v2 offset:4
	v_add_u32_e32 v2, v2, v3
	ds_write_b32 v1, v2 offset:8
	v_add_u32_e32 v2, v2, v3
	ds_write_b32 v1, v2 offset:12
	v_add_u32_e32 v2, v2, v3
	ds_write_b32 v1, v2 offset:16
	v_add_u32_e32 v2, v2, v3
	ds_write_b32 v1, v2 offset:20
	v_add_u32_e32 v2, v2, v3
	ds_write_b32 v1, v2 offset:24
	v_add_u32_e32 v2, v2, v3
	ds_write_b32 v1, v2 offset:28
	v_add_u32_e32 v2, v2, v3
	v_cmp_lt_i32_e32 vcc, 0, v5
	s_nop 1
	v_cndmask_b32_e64 v3, 0, 1, vcc
	ds_write_b32 v1, v2 offset:32
	v_add_u32_e32 v2, v2, v3
	ds_write_b32 v1, v2 offset:36
	v_add_u32_e32 v2, v2, v3
	ds_write_b32 v1, v2 offset:40
	v_add_u32_e32 v2, v2, v3
	ds_write_b32 v1, v2 offset:44
	v_add_u32_e32 v2, v2, v3
	ds_write_b32 v1, v2 offset:48
	v_add_u32_e32 v2, v2, v3
	ds_write_b32 v1, v2 offset:52
	v_add_u32_e32 v2, v2, v3
	ds_write_b32 v1, v2 offset:56
	v_add_u32_e32 v2, v2, v3
	v_cmp_lt_i32_e32 vcc, 0, v5
	s_nop 1
	v_addc_co_u32_e32 v3, vcc, 0, v4, vcc
	ds_write_b32 v1, v2 offset:60
	v_add_u32_e32 v2, v2, v3
	v_cmp_lt_i32_e32 vcc, 0, v6
	s_nop 1
	v_addc_co_u32_e32 v3, vcc, 0, v4, vcc
	ds_write_b32 v1, v2 offset:64
	v_add_u32_e32 v2, v2, v3
	ds_write_b32 v1, v2 offset:68
	v_add_u32_e32 v2, v2, v3
	ds_write_b32 v1, v2 offset:72
	v_add_u32_e32 v2, v2, v3
	ds_write_b32 v1, v2 offset:76
	v_add_u32_e32 v2, v2, v3
	ds_write_b32 v1, v2 offset:80
	v_add_u32_e32 v2, v2, v3
	ds_write_b32 v1, v2 offset:84
	v_add_u32_e32 v2, v2, v3
	ds_write_b32 v1, v2 offset:88
	v_add_u32_e32 v2, v2, v3
	v_cmp_lt_i32_e32 vcc, 0, v6
	s_nop 1
	v_addc_co_u32_e32 v3, vcc, 0, v5, vcc
	ds_write_b32 v1, v2 offset:92
	v_add_u32_e32 v2, v2, v3
	v_cmp_lt_i32_e32 vcc, 0, v7
	s_nop 1
	v_addc_co_u32_e32 v3, vcc, 0, v5, vcc
	ds_write_b32 v1, v2 offset:96
	v_add_u32_e32 v2, v2, v3
	ds_write_b32 v1, v2 offset:100
	v_add_u32_e32 v2, v2, v3
	ds_write_b32 v1, v2 offset:104
	v_add_u32_e32 v2, v2, v3
	ds_write_b32 v1, v2 offset:108
	v_add_u32_e32 v2, v2, v3
	ds_write_b32 v1, v2 offset:112
	v_add_u32_e32 v2, v2, v3
	ds_write_b32 v1, v2 offset:116
	v_add_u32_e32 v2, v2, v3
	ds_write_b32 v1, v2 offset:120
	v_add_u32_e32 v2, v2, v3
	v_cmp_lt_i32_e32 vcc, 0, v7
	s_nop 1
	v_addc_co_u32_e32 v3, vcc, 0, v6, vcc
	ds_write_b32 v1, v2 offset:124
	v_add_u32_e32 v2, v2, v3
	v_mov_b32_e32 v3, v6
	ds_write_b32 v1, v2 offset:128
	v_add_u32_e32 v2, v2, v3
	ds_write_b32 v1, v2 offset:132
	v_add_u32_e32 v2, v2, v3
	ds_write_b32 v1, v2 offset:136
	v_add_u32_e32 v2, v2, v3
	ds_write_b32 v1, v2 offset:140
	v_add_u32_e32 v2, v2, v3
	ds_write_b32 v1, v2 offset:144
	v_add_u32_e32 v2, v2, v3
	ds_write_b32 v1, v2 offset:148
	v_add_u32_e32 v2, v2, v3
	ds_write_b32 v1, v2 offset:152
	v_add_u32_e32 v2, v2, v3
	v_mov_b32_e32 v3, v7
	ds_write_b32 v1, v2 offset:156
	v_add_u32_e32 v2, v2, v3
	ds_write_b32 v1, v2 offset:160
	v_add_u32_e32 v2, v2, v3
	ds_write_b32 v1, v2 offset:164
	v_add_u32_e32 v2, v2, v3
	ds_write_b32 v1, v2 offset:168
	v_add_u32_e32 v2, v2, v3
	ds_write_b32 v1, v2 offset:172
	v_add_u32_e32 v2, v2, v3
	ds_write_b32 v1, v2 offset:176
	v_add_u32_e32 v2, v2, v3
	ds_write_b32 v1, v2 offset:180
	v_add_u32_e32 v2, v2, v3
	ds_write_b32 v1, v2 offset:184
	v_add_u32_e32 v2, v2, v3
	ds_write_b32 v1, v2 offset:188
